# GQA units keep 24 rider trips but tiles 12..23 are redirected to dummies there and converted by the differential units
# baseline (speedup 1.0000x reference)
; DI f32x16 mfma8(v8i a, v8i b, f32x16 c) { return __builtin_amdgcn_mfma_scale_f32_32x32x64_f8f6f4(a, b, c, 0, 0, 0, 0, 0, 0); }
; DI void attn_unit_d8(unsigned char* lds, const AttnArgs& a) {
;     ...
;     auto tile = [&](const unsigned char* Kb, const unsigned char* Kn, v8i& Pa, v8i& Pb, v8i& v0, v8i& v1, const v8i& Qa, const v8i& Qb, const v8i& w0, const v8i& w1) __attribute__((always_inline)) {
;         qk(Kb, 1, s1a, s1b);
;         v0 = rd32(Kb + voff); v1 = rd32(Kb + voff + 32 * A8_PITCH);
;         o0[0] = mfma8(w0, Qa, o0[0]); o1[0] = mfma8(w0, Qb, o1[0]); o0[1] = mfma8(w1, Qa, o0[1]); o1[1] = mfma8(w1, Qb, o1[1]);
;         expsum(s0a, l0); expsum(s0b, l1); pack4(s0a, Pa, 0); pack4(s0b, Pb, 0);
;         qk(Kn, 0, s0a, s0b);
;         expsum(s1a, l0); expsum(s1b, l1); pack4(s1a, Pa, 4); pack4(s1b, Pb, 4);
; #pragma unroll
;         for (int i = 0; i < 8; ++i) { __builtin_amdgcn_sched_group_barrier(0x008, 1, 0); __builtin_amdgcn_sched_group_barrier(0x402, 22, 0); }
;     };
;     for (int t = a.t0; t < a.t1; t += 2) {
;         const int s1 = sb + 1 >= 5 ? sb - 4 : sb + 1, s2 = sb + 2 >= 5 ? sb - 3 : sb + 2, s3 = sb + 3 >= 5 ? sb - 2 : sb + 3, s4 = sb + 4 >= 5 ? sb - 1 : sb + 4;
;         { const int ta = t + 3, tb = t + 4; gload(ta < a.t1 ? ta : a.t1 - 1, kreg0, vreg0); gload(tb < a.t1 ? tb : a.t1 - 1, kreg1, vreg1); }
;         tile(lds + sb * D8_SLOT, lds + s1 * D8_SLOT, PaX, PbX, vX0, vX1, PaY, PbY, vY0, vY1);
.LBB0_663:
	s_cmp_gt_i32 s16, 3
	s_cselect_b32 s17, -4, 1
	s_add_i32 s18, s17, s16
	s_mul_i32 s6, s16, 0x2800
	s_cmp_gt_i32 s16, 2
	v_mfma_f32_32x32x64_f8f6f4 v[50:65], v[154:161], v[138:145], v[50:65]
	v_exp_f32_e32 v192, v90
	v_add_u32_e32 v90, s6, v218
	s_cselect_b32 s6, -3, 2
	s_add_i32 s6, s6, s16
	s_cmp_gt_i32 s16, 1
	s_cselect_b32 s19, -2, 3
	s_add_i32 s19, s19, s16
	s_cmp_gt_i32 s16, 0
	s_cselect_b32 s49, -1, 4
	s_min_u32 s54, s46, 64
	s_add_i32 s49, s49, s16
	s_cmp_lt_u32 s46, 61
	s_mul_i32 s17, s6, 0x2800
	s_mov_b32 s16, s6
	s_cselect_b64 s[52:53], -1, 0
	s_lshl_b32 s6, s54, 6
	s_add_i32 s54, s6, 0xc0
	s_add_i32 s55, s6, 0xfffff0c0
	s_and_b64 s[52:53], s[52:53], exec
	v_lshl_add_u64 v[98:99], v[182:183], 0, s[6:7]
	s_cselect_b32 s6, s54, s55
	s_cselect_b32 s53, s21, s48
	s_cselect_b32 s52, s20, s47
	s_min_u32 s56, s46, 63
	v_exp_f32_e32 v198, v82
	v_exp_f32_e32 v199, v83
	v_exp_f32_e32 v196, v84
	v_exp_f32_e32 v197, v85
	v_exp_f32_e32 v200, v86
	v_exp_f32_e32 v201, v87
	v_exp_f32_e32 v194, v88
	v_exp_f32_e32 v195, v89
	ds_read_b128 v[82:85], v90 offset:2560
	ds_read_b128 v[86:89], v90 offset:2576
	global_load_dwordx2 v[202:203], v[98:99], off offset:192
	v_add_u32_e32 v98, s6, v215
	s_cmp_lt_u32 s46, 60
	v_ashrrev_i32_e32 v99, 31, v98
	s_cselect_b64 s[54:55], -1, 0
	s_lshl_b32 s6, s56, 6
	v_lshlrev_b64 v[98:99], 8, v[98:99]
	s_add_i32 s56, s6, 0x100
	s_add_i32 s57, s6, 0xfffff100
	v_lshl_add_u64 v[98:99], s[52:53], 0, v[98:99]
	s_and_b64 s[52:53], s[54:55], exec
	s_cselect_b32 s54, s56, s57
	v_lshl_add_u64 v[220:221], v[98:99], 0, v[178:179]
	v_add_u32_e32 v98, s54, v215
	v_ashrrev_i32_e32 v99, 31, v98
	s_cselect_b32 s53, s21, s48
	s_cselect_b32 s52, s20, s47
	v_lshlrev_b64 v[98:99], 8, v[98:99]
	v_lshl_add_u64 v[100:101], v[182:183], 0, s[6:7]
	v_lshl_add_u64 v[98:99], s[52:53], 0, v[98:99]
	global_load_dwordx2 v[204:205], v[100:101], off offset:256
	v_lshl_add_u64 v[222:223], v[98:99], 0, v[178:179]
	s_waitcnt lgkmcnt(0)
	v_mfma_f32_32x32x64_f8f6f4 v[98:113], v[82:89], v[114:121], 0
	v_exp_f32_e32 v193, v91
	v_exp_f32_e32 v224, v92
	v_exp_f32_e32 v225, v93
	v_exp_f32_e32 v226, v94
	v_exp_f32_e32 v227, v95
	v_exp_f32_e32 v228, v96
	v_exp_f32_e32 v229, v97
	ds_read_b128 v[170:173], v90 offset:5120
	ds_read_b128 v[174:177], v90 offset:5136
	ds_read_b128 v[162:165], v90 offset:7680
	ds_read_b128 v[166:169], v90 offset:7696
	v_pk_add_f32 v[90:91], v[186:187], v[198:199]
	v_pk_add_f32 v[92:93], v[184:185], v[196:197]
	v_pk_add_f32 v[90:91], v[200:201], v[90:91]
	v_pk_add_f32 v[92:93], v[194:195], v[92:93]
	v_pk_add_f32 v[90:91], v[192:193], v[90:91]
	v_pk_add_f32 v[92:93], v[224:225], v[92:93]
	v_exp_f32_e32 v66, v66
	v_exp_f32_e32 v67, v67
	v_exp_f32_e32 v68, v68
	v_exp_f32_e32 v69, v69
	v_exp_f32_e32 v70, v70
	v_exp_f32_e32 v71, v71
	v_exp_f32_e32 v72, v72
	v_pk_add_f32 v[230:231], v[228:229], v[92:93]
	v_pk_add_f32 v[232:233], v[226:227], v[90:91]
	v_mfma_f32_32x32x64_f8f6f4 v[82:97], v[82:89], v[122:129], 0
	v_exp_f32_e32 v73, v73
	v_exp_f32_e32 v74, v74
	v_exp_f32_e32 v75, v75
	v_exp_f32_e32 v76, v76
	v_exp_f32_e32 v77, v77
	v_exp_f32_e32 v78, v78
	v_exp_f32_e32 v79, v79
	v_exp_f32_e32 v80, v80
	v_exp_f32_e32 v81, v81
	v_pk_add_f32 v[186:187], v[190:191], v[66:67]
	v_pk_add_f32 v[188:189], v[188:189], v[68:69]
	s_nop 0
	v_pk_add_f32 v[186:187], v[70:71], v[186:187]
	v_pk_add_f32 v[188:189], v[72:73], v[188:189]
	s_nop 0
	v_cvt_scalef32_pk_fp8_f32 v184, v198, v199, s36
	v_pk_add_f32 v[186:187], v[74:75], v[186:187]
	v_pk_add_f32 v[188:189], v[76:77], v[188:189]
	v_cvt_scalef32_pk_fp8_f32 v185, v200, v201, s36
	v_cvt_scalef32_pk_fp8_f32 v184, v196, v197, s36 op_sel:[0,0,0,1]
	v_pk_add_f32 v[190:191], v[78:79], v[186:187]
	v_pk_add_f32 v[188:189], v[80:81], v[188:189]
	v_mfma_f32_32x32x64_f8f6f4 v[2:17], v[154:161], v[130:137], v[2:17]
	s_nop 0
	s_nop 0
	s_nop 0
	s_nop 0
	s_nop 0
	s_nop 0
	s_mulk_i32 s18, 0x2800
	v_cvt_scalef32_pk_fp8_f32 v186, v192, v193, s36
	v_cvt_scalef32_pk_fp8_f32 v187, v226, v227, s36
	v_cvt_scalef32_pk_fp8_f32 v154, v66, v67, s36
	v_cvt_scalef32_pk_fp8_f32 v155, v70, v71, s36
	v_cvt_scalef32_pk_fp8_f32 v156, v74, v75, s36
	v_cvt_scalef32_pk_fp8_f32 v157, v78, v79, s36
	v_cvt_scalef32_pk_fp8_f32 v185, v194, v195, s36 op_sel:[0,0,0,1]
	v_add_u32_e32 v219, s18, v218
	v_cvt_scalef32_pk_fp8_f32 v186, v224, v225, s36 op_sel:[0,0,0,1]
	v_cvt_scalef32_pk_fp8_f32 v187, v228, v229, s36 op_sel:[0,0,0,1]
	v_cvt_scalef32_pk_fp8_f32 v154, v68, v69, s36 op_sel:[0,0,0,1]
	v_cvt_scalef32_pk_fp8_f32 v155, v72, v73, s36 op_sel:[0,0,0,1]
	v_cvt_scalef32_pk_fp8_f32 v156, v76, v77, s36 op_sel:[0,0,0,1]
	v_cvt_scalef32_pk_fp8_f32 v157, v80, v81, s36 op_sel:[0,0,0,1]
	v_exp_f32_e32 v98, v98
	v_exp_f32_e32 v99, v99
	v_mfma_f32_32x32x64_f8f6f4 v[34:49], v[146:153], v[138:145], v[34:49]
	v_exp_f32_e32 v100, v100
	v_exp_f32_e32 v101, v101
	v_exp_f32_e32 v102, v102
	v_exp_f32_e32 v103, v103
	v_exp_f32_e32 v104, v104
	v_exp_f32_e32 v105, v105
	v_exp_f32_e32 v106, v106
	v_exp_f32_e32 v107, v107
	v_exp_f32_e32 v108, v108
	v_exp_f32_e32 v109, v109
	v_exp_f32_e32 v110, v110
	v_exp_f32_e32 v111, v111
	v_exp_f32_e32 v112, v112
	v_exp_f32_e32 v113, v113
	ds_read_b128 v[192:195], v219
	ds_read_b128 v[196:199], v219 offset:16
	v_pk_add_f32 v[66:67], v[232:233], v[98:99]
	v_pk_add_f32 v[68:69], v[230:231], v[100:101]
	v_pk_add_f32 v[66:67], v[102:103], v[66:67]
	v_pk_add_f32 v[68:69], v[104:105], v[68:69]
	v_pk_add_f32 v[66:67], v[106:107], v[66:67]
	v_pk_add_f32 v[68:69], v[108:109], v[68:69]
	v_pk_add_f32 v[140:141], v[110:111], v[66:67]
	v_pk_add_f32 v[138:139], v[112:113], v[68:69]
	v_mfma_f32_32x32x64_f8f6f4 v[18:33], v[146:153], v[130:137], v[18:33]
	v_exp_f32_e32 v82, v82
	v_exp_f32_e32 v83, v83
	v_exp_f32_e32 v84, v84
	v_exp_f32_e32 v85, v85
	v_exp_f32_e32 v86, v86
	v_exp_f32_e32 v87, v87
	v_exp_f32_e32 v88, v88
	v_exp_f32_e32 v89, v89
	v_exp_f32_e32 v90, v90
	v_exp_f32_e32 v91, v91
	v_exp_f32_e32 v92, v92
	v_exp_f32_e32 v93, v93
	v_exp_f32_e32 v94, v94
	v_exp_f32_e32 v95, v95
	v_exp_f32_e32 v96, v96
	v_exp_f32_e32 v97, v97
	v_pk_add_f32 v[66:67], v[190:191], v[82:83]
	v_pk_add_f32 v[68:69], v[188:189], v[84:85]
	v_pk_add_f32 v[66:67], v[86:87], v[66:67]
	v_pk_add_f32 v[68:69], v[88:89], v[68:69]
	v_pk_add_f32 v[130:131], v[90:91], v[66:67]
	v_pk_add_f32 v[132:133], v[92:93], v[68:69]
	s_waitcnt lgkmcnt(0)
; DI KParamsPtr kparams() { KParamsPtr p = (KParamsPtr)__builtin_amdgcn_kernarg_segment_ptr(); asm volatile("" : "+s"(p)); return p; }
; DI void attn_unit_a8(unsigned char* lds, const AttnArgs& a) {
;     ...
;     auto w_decode = [&](int j, const float*& src, unsigned char*& dst, int& ld, int& n0, int& k0, bool& gu) __attribute__((always_inline)) {
;         const int g = (j >> 2) * 512 + a.wl, e = g / 96, rr = g - e * 96; KParamsPtr kp = kparams();
;         if (rr < 64) { src = kp->w_gu + ((size_t)a.wli * NE + e) * (1024 * 2048); dst = kp->ws + WS_WGU + (size_t)a.wli * SZ_WGU + (size_t)e * 2048 * 1024; ld = 2048; n0 = (rr & 7) * 256; k0 = ((rr >> 3) * 4 + (j & 3)) * 32; gu = true; }
;         else { const int q = rr - 64; src = kp->w_dn + ((size_t)a.wli * NE + e) * (1024 * 1024); dst = kp->ws + WS_WDN + (size_t)a.wli * SZ_WDN + (size_t)e * 1024 * 1024; ld = 1024; n0 = (q & 3) * 256; k0 = ((q >> 2) * 4 + (j & 3)) * 32; gu = false; } };
;     auto w_issue = [&](int j) __attribute__((always_inline)) { const float* src; unsigned char* dst; int ld, n0, k0; bool gu; w_decode(j, src, dst, ld, n0, k0, gu);
;         const float* p = src + (size_t)(k0 + 4 * wid) * ld + n0 + wn4;
;         wq[0] = __builtin_nontemporal_load((const f32x4*)p); wq[1] = __builtin_nontemporal_load((const f32x4*)(p + ld));
;         wq[2] = __builtin_nontemporal_load((const f32x4*)(p + (size_t)2 * ld)); wq[3] = __builtin_nontemporal_load((const f32x4*)(p + (size_t)3 * ld)); };
; DI void attn_unit_d8(unsigned char* lds, const AttnArgs& a) {
;     ...
;     auto tile = [&](const unsigned char* Kb, const unsigned char* Kn, v8i& Pa, v8i& Pb, v8i& v0, v8i& v1, const v8i& Qa, const v8i& Qb, const v8i& w0, const v8i& w1) __attribute__((always_inline)) {
;         qk(Kb, 1, s1a, s1b);
;         v0 = rd32(Kb + voff); v1 = rd32(Kb + voff + 32 * A8_PITCH);
;         o0[0] = mfma8(w0, Qa, o0[0]); o1[0] = mfma8(w0, Qb, o1[0]); o0[1] = mfma8(w1, Qa, o0[1]); o1[1] = mfma8(w1, Qb, o1[1]);
;         expsum(s0a, l0); expsum(s0b, l1); pack4(s0a, Pa, 0); pack4(s0b, Pb, 0);
;         qk(Kn, 0, s0a, s0b);
;         expsum(s1a, l0); expsum(s1b, l1); pack4(s1a, Pa, 4); pack4(s1b, Pb, 4);
; #pragma unroll
;         for (int i = 0; i < 8; ++i) { __builtin_amdgcn_sched_group_barrier(0x008, 1, 0); __builtin_amdgcn_sched_group_barrier(0x402, 22, 0); }
;     };
	v_mfma_f32_32x32x64_f8f6f4 v[66:81], v[192:199], v[114:121], 0
	s_nop 0
	s_nop 0
	s_nop 0
	s_nop 0
	s_nop 0
	s_nop 0
	s_nop 0
	v_cvt_scalef32_pk_fp8_f32 v188, v98, v99, s36
	v_cvt_scalef32_pk_fp8_f32 v189, v102, v103, s36
	v_cvt_scalef32_pk_fp8_f32 v190, v106, v107, s36
	v_cvt_scalef32_pk_fp8_f32 v191, v110, v111, s36
	v_cvt_scalef32_pk_fp8_f32 v158, v82, v83, s36
	v_cvt_scalef32_pk_fp8_f32 v159, v86, v87, s36
	v_pk_add_f32 v[142:143], v[96:97], v[132:133]
	v_pk_add_f32 v[144:145], v[94:95], v[130:131]
	v_cvt_scalef32_pk_fp8_f32 v160, v90, v91, s36
	v_cvt_scalef32_pk_fp8_f32 v188, v100, v101, s36 op_sel:[0,0,0,1]
	v_cvt_scalef32_pk_fp8_f32 v189, v104, v105, s36 op_sel:[0,0,0,1]
	v_cvt_scalef32_pk_fp8_f32 v190, v108, v109, s36 op_sel:[0,0,0,1]
	v_cvt_scalef32_pk_fp8_f32 v191, v112, v113, s36 op_sel:[0,0,0,1]
	v_cvt_scalef32_pk_fp8_f32 v158, v84, v85, s36 op_sel:[0,0,0,1]
	v_cvt_scalef32_pk_fp8_f32 v159, v88, v89, s36 op_sel:[0,0,0,1]
	v_mfma_f32_32x32x64_f8f6f4 v[98:113], v[192:199], v[122:129], 0
	global_load_dwordx2 v[192:193], v[220:221], off
	global_load_dwordx2 v[194:195], v[222:223], off
	ds_read_b128 v[130:133], v219 offset:2560
	ds_read_b128 v[134:137], v219 offset:2576
	s_mulk_i32 s19, 0x2800
	s_nop 0
	v_exp_f32_e32 v146, v66
	s_add_i32 s80, s61, 12
	v_exp_f32_e32 v147, v67
	s_lshr_b32 s73, s80, 2
	v_exp_f32_e32 v148, v68
	s_lshl_b32 s73, s73, 9
	v_exp_f32_e32 v149, v69
	s_add_i32 s73, s73, s42
	s_add_i32 s19, s19, 0
	v_cvt_scalef32_pk_fp8_f32 v161, v94, v95, s36
	v_exp_f32_e32 v150, v70
	s_mul_i32 s75, s73, 0xaaab
	v_exp_f32_e32 v151, v71
	s_lshr_b32 s75, s75, 22
	v_exp_f32_e32 v152, v72
	s_mul_i32 s76, s75, 0x60
	v_exp_f32_e32 v153, v73
	s_sub_i32 s76, s73, s76
	v_add_u32_e32 v224, s19, v216
	v_add_u32_e32 v225, s19, v217
	v_cvt_scalef32_pk_fp8_f32 v160, v92, v93, s36 op_sel:[0,0,0,1]
	v_cvt_scalef32_pk_fp8_f32 v161, v96, v97, s36 op_sel:[0,0,0,1]
	v_exp_f32_e32 v196, v74
	s_lshr_b32 s77, s76, 6
	v_exp_f32_e32 v197, v75
	s_lshl_b32 s78, s77, 6
	v_exp_f32_e32 v198, v76
	s_sub_i32 s76, s76, s78
	v_exp_f32_e32 v199, v77
	s_sub_i32 s78, 3, s77
	v_exp_f32_e32 v200, v78
	s_lshr_b32 s79, s76, s78
	v_exp_f32_e32 v201, v79
	s_lshl_b32 s79, s79, 2
	v_exp_f32_e32 v220, v80
	s_and_b32 s81, s80, 3
	v_exp_f32_e32 v221, v81
	s_add_i32 s79, s79, s81
	s_waitcnt lgkmcnt(0)
	v_mfma_f32_32x32x64_f8f6f4 v[82:97], v[130:137], v[114:121], 0
	v_add_f32_e64 v66, v140, v146
	v_add_f32_e64 v67, v141, v147
	v_add_f32_e64 v68, v138, v148
	v_add_f32_e64 v69, v139, v149
	v_add_f32_e64 v66, v150, v66
	v_add_f32_e64 v67, v151, v67
	v_add_f32_e64 v68, v152, v68
	v_add_f32_e64 v69, v153, v69
	v_add_f32_e64 v138, v196, v66
	v_add_f32_e64 v139, v197, v67
	v_add_f32_e64 v140, v198, v68
	v_add_f32_e64 v141, v199, v69
	v_exp_f32_e32 v98, v98
	s_lshl_b32 s79, s79, 5
	v_exp_f32_e32 v99, v99
	s_lshl_b32 s81, s63, 2
	v_exp_f32_e32 v100, v100
	s_add_i32 s81, s81, s79
	v_exp_f32_e32 v101, v101
	s_sub_i32 s78, 13, s77
	v_exp_f32_e32 v102, v102
	s_lshl_b32 s81, s81, s78
	v_exp_f32_e32 v103, v103
	s_lshr_b32 s78, 7, s77
	v_exp_f32_e32 v104, v104
	s_and_b32 s78, s76, s78
	v_exp_f32_e32 v105, v105
	s_lshl_b32 s72, s78, 10
	v_exp_f32_e32 v106, v106
	s_add_i32 s81, s81, s72
	v_exp_f32_e32 v107, v107
	s_add_i32 s72, s75, 0
	v_exp_f32_e32 v108, v108
	s_sub_i32 s80, 23, s77
	v_exp_f32_e32 v109, v109
	s_lshl_b32 s72, s72, s80
	v_exp_f32_e32 v110, v110
	s_add_i32 s81, s81, s72
	v_exp_f32_e32 v111, v111
	s_cmp_eq_u32 s77, 0
	s_cselect_b64 s[84:85], s[66:67], s[68:69]
	v_exp_f32_e32 v112, v112
	s_add_u32 s84, s84, s81
	s_addc_u32 s85, s85, 0
	v_exp_f32_e32 v113, v113
	s_lshr_b32 s80, 0x2000, s77
	v_mfma_f32_32x32x64_f8f6f4 v[66:81], v[130:137], v[122:129], 0
	v_add_f32_e64 v130, v144, v98
	v_add_f32_e64 v131, v145, v99
	v_add_f32_e64 v132, v142, v100
	v_add_f32_e64 v133, v143, v101
	v_add_f32_e64 v142, v102, v130
	v_add_f32_e64 v143, v103, v131
	v_add_f32_e64 v132, v104, v132
	v_add_f32_e64 v133, v105, v133
	v_add_f32_e64 v134, v220, v140
	v_add_f32_e64 v135, v221, v141
	v_add_f32_e64 v136, v200, v138
	v_add_f32_e64 v137, v201, v139
	s_nop 0
	s_nop 0
	s_nop 0
	s_nop 0
	s_nop 0
	s_nop 0
	v_pk_add_f32 v[142:143], v[106:107], v[142:143]
	v_pk_add_f32 v[132:133], v[108:109], v[132:133]
	v_cvt_scalef32_pk_fp8_f32 v138, v146, v147, s36
	v_cvt_scalef32_pk_fp8_f32 v139, v150, v151, s36
	v_cvt_scalef32_pk_fp8_f32 v140, v196, v197, s36
	v_cvt_scalef32_pk_fp8_f32 v141, v200, v201, s36
	v_cvt_scalef32_pk_fp8_f32 v130, v98, v99, s36
	v_cvt_scalef32_pk_fp8_f32 v131, v102, v103, s36
	v_pk_add_f32 v[146:147], v[112:113], v[132:133]
	v_pk_add_f32 v[150:151], v[110:111], v[142:143]
	v_mfma_f32_32x32x64_f8f6f4 v[50:65], v[170:177], v[184:191], v[50:65]
	v_exp_f32_e32 v82, v82
	s_and_b32 s72, s78, 3
	v_exp_f32_e32 v83, v83
	s_lshl_b32 s72, s72, 19
	v_exp_f32_e32 v84, v84
	s_lshr_b32 s81, s78, 2
; DI unsigned pk4_fp8_mul64(float a, float b, float c, float d) { v2s_t r = {0, 0}; r = __builtin_amdgcn_cvt_scalef32_pk_fp8_f32(r, a, b, 0.015625f, false); r = __builtin_amdgcn_cvt_scalef32_pk_fp8_f32(r, c, d, 0.015625f, true); return __builtin_bit_cast(unsigned, r); }
; DI f32x16 mfma8(v8i a, v8i b, f32x16 c) { return __builtin_amdgcn_mfma_scale_f32_32x32x64_f8f6f4(a, b, c, 0, 0, 0, 0, 0, 0); }
; DI void attn_unit_a8(unsigned char* lds, const AttnArgs& a) {
;     ...
;     auto w_cvt = [&]() __attribute__((always_inline)) { unsigned char* t8 = lds + AT_WT + wn4 * WPITCH + 4 * wid;
; #pragma unroll
;         for (int j = 0; j < 4; ++j) *(unsigned*)(t8 + j * WPITCH) = pk4_fp8_mul64(wq[0][j], wq[1][j], wq[2][j], wq[3][j]); };
;     const int wcol = tid >> 1, whalf = tid & 1;
;     const unsigned wper_gu = (unsigned)((wcol >> 7) * 256 + (wcol & 96) + invperm32(wcol & 31)) * 1024u + 16u * whalf;
;     const unsigned wper_dn = (unsigned)fwd_lane16(wcol) * 1024u + 16u * whalf;
;     auto w_store = [&](int j) __attribute__((always_inline)) { const float* src; unsigned char* dst; int ld, n0, k0; bool gu; w_decode(j, src, dst, ld, n0, k0, gu);
;         const int nb = n0 >> 8; const unsigned uni = (unsigned)(gu ? (nb & 3) * 512 + (nb >> 2) * 128 : nb * 256) * 1024u + (unsigned)k0;
;         const unsigned off = (gu ? wper_gu : wper_dn) + uni;
;         const unsigned* t = (const unsigned*)(lds + AT_WT + wcol * WPITCH + 16 * whalf);
;         *(u32x4*)(dst + off) = (u32x4){t[0], t[1], t[2], t[3]}; };
; DI void attn_unit_d8(unsigned char* lds, const AttnArgs& a) {
;     ...
;     auto tile = [&](const unsigned char* Kb, const unsigned char* Kn, v8i& Pa, v8i& Pb, v8i& v0, v8i& v1, const v8i& Qa, const v8i& Qb, const v8i& w0, const v8i& w1) __attribute__((always_inline)) {
;         qk(Kb, 1, s1a, s1b);
;         v0 = rd32(Kb + voff); v1 = rd32(Kb + voff + 32 * A8_PITCH);
;         o0[0] = mfma8(w0, Qa, o0[0]); o1[0] = mfma8(w0, Qb, o1[0]); o0[1] = mfma8(w1, Qa, o0[1]); o1[1] = mfma8(w1, Qb, o1[1]);
;         expsum(s0a, l0); expsum(s0b, l1); pack4(s0a, Pa, 0); pack4(s0b, Pb, 0);
;         qk(Kn, 0, s0a, s0b);
;         expsum(s1a, l0); expsum(s1b, l1); pack4(s1a, Pa, 4); pack4(s1b, Pb, 4);
; #pragma unroll
;         for (int i = 0; i < 8; ++i) { __builtin_amdgcn_sched_group_barrier(0x008, 1, 0); __builtin_amdgcn_sched_group_barrier(0x402, 22, 0); }
;     };
	v_exp_f32_e32 v85, v85
	s_lshl_b32 s81, s81, 17
	v_add_u32_e32 v102, s17, v218
	v_exp_f32_e32 v86, v86
	s_add_i32 s72, s72, s81
	v_exp_f32_e32 v87, v87
	s_lshl_b32 s81, s78, 18
	v_exp_f32_e32 v88, v88
	s_cmp_eq_u32 s77, 0
	s_cselect_b32 s72, s72, s81
	v_exp_f32_e32 v89, v89
	s_mul_i32 s81, s77, 0x10000000
	v_cvt_scalef32_pk_fp8_f32 v130, v100, v101, s36 op_sel:[0,0,0,1]
	v_cvt_scalef32_pk_fp8_f32 v131, v104, v105, s36 op_sel:[0,0,0,1]
	v_exp_f32_e32 v90, v90
	s_add_i32 s81, s81, 0x1094000
	v_exp_f32_e32 v91, v91
	s_add_i32 s72, s72, s79
	v_exp_f32_e32 v92, v92
	s_sub_i32 s73, 21, s77
	v_exp_f32_e32 v93, v93
	s_lshl_b32 s73, s75, s73
	ds_read_b128 v[98:101], v102
	ds_read_b128 v[102:105], v102 offset:16
	s_nop 0
	v_cvt_scalef32_pk_fp8_f32 v138, v148, v149, s36 op_sel:[0,0,0,1]
	v_cvt_scalef32_pk_fp8_f32 v139, v152, v153, s36 op_sel:[0,0,0,1]
	v_cvt_scalef32_pk_fp8_f32 v140, v198, v199, s36 op_sel:[0,0,0,1]
	v_cvt_scalef32_pk_fp8_f32 v141, v220, v221, s36 op_sel:[0,0,0,1]
	s_nop 0
	v_exp_f32_e32 v94, v94
	s_add_i32 s72, s72, s73
	v_mfma_f32_32x32x64_f8f6f4 v[2:17], v[170:177], v[154:161], v[2:17]
	v_exp_f32_e32 v148, v96
	s_add_u32 s72, s72, s81
	v_cvt_scalef32_pk_fp8_f32 v132, v106, v107, s36
	v_exp_f32_e32 v149, v97
	s_or_b32 s79, s72, s77
	v_pk_add_f32 v[96:97], v[136:137], v[82:83]
	v_pk_add_f32 v[106:107], v[134:135], v[84:85]
	v_exp_f32_e32 v66, v66
	v_exp_f32_e32 v67, v67
	v_exp_f32_e32 v68, v68
	v_exp_f32_e32 v69, v69
	v_exp_f32_e32 v95, v95
	v_cvt_scalef32_pk_fp8_f32 v133, v110, v111, s36
	v_pk_add_f32 v[106:107], v[88:89], v[106:107]
	v_pk_add_f32 v[96:97], v[86:87], v[96:97]
	v_exp_f32_e32 v70, v70
	v_exp_f32_e32 v71, v71
	v_exp_f32_e32 v72, v72
	v_exp_f32_e32 v73, v73
	v_cvt_scalef32_pk_fp8_f32 v132, v108, v109, s36 op_sel:[0,0,0,1]
	v_cvt_scalef32_pk_fp8_f32 v133, v112, v113, s36 op_sel:[0,0,0,1]
	v_pk_add_f32 v[96:97], v[90:91], v[96:97]
	v_pk_add_f32 v[106:107], v[92:93], v[106:107]
	v_exp_f32_e32 v74, v74
	v_mfma_f32_32x32x64_f8f6f4 v[34:49], v[162:169], v[184:191], v[34:49]
	v_exp_f32_e32 v75, v75
	v_exp_f32_e32 v76, v76
	v_exp_f32_e32 v77, v77
	v_exp_f32_e32 v78, v78
	v_exp_f32_e32 v79, v79
	s_nop 0
	v_exp_f32_e32 v80, v80
	v_exp_f32_e32 v81, v81
	s_nop 0
	s_nop 0
	v_cvt_scalef32_pk_fp8_f32 v142, v82, v83, s36
	s_nop 0
	v_cvt_scalef32_pk_fp8_f32 v143, v86, v87, s36
	v_cvt_scalef32_pk_fp8_f32 v144, v90, v91, s36
	v_cvt_scalef32_pk_fp8_f32 v142, v84, v85, s36 op_sel:[0,0,0,1]
	v_pk_add_f32 v[82:83], v[150:151], v[66:67]
	v_pk_add_f32 v[84:85], v[146:147], v[68:69]
	s_mulk_i32 s49, 0x2800
	v_pk_add_f32 v[184:185], v[148:149], v[106:107]
	v_pk_add_f32 v[186:187], v[94:95], v[96:97]
	v_cvt_scalef32_pk_fp8_f32 v145, v94, v95, s36
	v_cvt_scalef32_pk_fp8_f32 v143, v88, v89, s36 op_sel:[0,0,0,1]
	v_cvt_scalef32_pk_fp8_f32 v144, v92, v93, s36 op_sel:[0,0,0,1]
	v_mfma_f32_32x32x64_f8f6f4 v[18:33], v[162:169], v[154:161], v[18:33]
	v_add_f32_e64 v84, v72, v84
	v_add_f32_e64 v85, v73, v85
	v_add_f32_e64 v82, v70, v82
	v_add_f32_e64 v83, v71, v83
	s_nop 0
	s_nop 0
	s_nop 0
	s_nop 0
	s_add_i32 s6, s49, 0
	v_add_f32_e64 v82, v74, v82
	v_add_f32_e64 v83, v75, v83
	v_add_f32_e64 v84, v76, v84
	v_add_f32_e64 v85, v77, v85
	v_cvt_scalef32_pk_fp8_f32 v134, v66, v67, s36
	v_cvt_scalef32_pk_fp8_f32 v135, v70, v71, s36
	v_cvt_scalef32_pk_fp8_f32 v136, v74, v75, s36
	v_cvt_scalef32_pk_fp8_f32 v137, v78, v79, s36
	v_pk_add_f32 v[188:189], v[80:81], v[84:85]
	v_pk_add_f32 v[190:191], v[78:79], v[82:83]
	v_add_u32_e32 v106, s6, v216
	v_add_u32_e32 v107, s6, v217
	v_cvt_scalef32_pk_fp8_f32 v145, v148, v149, s36 op_sel:[0,0,0,1]
	v_cvt_scalef32_pk_fp8_f32 v134, v68, v69, s36 op_sel:[0,0,0,1]
	v_cvt_scalef32_pk_fp8_f32 v135, v72, v73, s36 op_sel:[0,0,0,1]
	v_cvt_scalef32_pk_fp8_f32 v136, v76, v77, s36 op_sel:[0,0,0,1]
	v_cvt_scalef32_pk_fp8_f32 v137, v80, v81, s36 op_sel:[0,0,0,1]
	s_waitcnt lgkmcnt(0)
	v_mfma_f32_32x32x64_f8f6f4 v[82:97], v[98:105], v[114:121], 0
	ds_read_b128 v[154:157], v219 offset:5120
	ds_read_b128 v[158:161], v219 offset:5136
	ds_read_b128 v[146:149], v219 offset:7680
	ds_read_b128 v[150:153], v219 offset:7696
	s_cmpk_gt_i32 s42, 0x1ff
	s_cbranch_scc1 .Lmy_rd0_ldum
	s_add_i32 s72, s61, -1
	s_cmp_lt_u32 s72, 12
	s_cbranch_scc0 .Lmy_rd0_noc
	s_waitcnt vmcnt(4)
	v_cvt_scalef32_pk_fp8_f32 v236, v236, v240, s62
	v_cvt_scalef32_pk_fp8_f32 v237, v237, v241, s62
	v_cvt_scalef32_pk_fp8_f32 v238, v238, v242, s62
	v_cvt_scalef32_pk_fp8_f32 v239, v239, v243, s62
	v_cvt_scalef32_pk_fp8_f32 v236, v244, v248, s62 op_sel:[0,0,0,1]
	v_cvt_scalef32_pk_fp8_f32 v237, v245, v249, s62 op_sel:[0,0,0,1]
	v_cvt_scalef32_pk_fp8_f32 v238, v246, v250, s62 op_sel:[0,0,0,1]
	v_cvt_scalef32_pk_fp8_f32 v239, v247, v251, s62 op_sel:[0,0,0,1]
	ds_write_b32 v252, v236
	ds_write_b32 v252, v237 offset:36
	ds_write_b32 v252, v238 offset:72
	ds_write_b32 v252, v239 offset:108

; DI void attn_unit_a8(unsigned char* lds, const AttnArgs& a) {
;     ...
;     auto w_issue = [&](int j) __attribute__((always_inline)) { const float* src; unsigned char* dst; int ld, n0, k0; bool gu; w_decode(j, src, dst, ld, n0, k0, gu);
;         const float* p = src + (size_t)(k0 + 4 * wid) * ld + n0 + wn4;
;         wq[0] = __builtin_nontemporal_load((const f32x4*)p); wq[1] = __builtin_nontemporal_load((const f32x4*)(p + ld));
;         wq[2] = __builtin_nontemporal_load((const f32x4*)(p + (size_t)2 * ld)); wq[3] = __builtin_nontemporal_load((const f32x4*)(p + (size_t)3 * ld)); };
;     auto w_cvt = [&]() __attribute__((always_inline)) { unsigned char* t8 = lds + AT_WT + wn4 * WPITCH + 4 * wid;
; #pragma unroll
;         for (int j = 0; j < 4; ++j) *(unsigned*)(t8 + j * WPITCH) = pk4_fp8_mul64(wq[0][j], wq[1][j], wq[2][j], wq[3][j]); };
;     const int wcol = tid >> 1, whalf = tid & 1;
;     const unsigned wper_gu = (unsigned)((wcol >> 7) * 256 + (wcol & 96) + invperm32(wcol & 31)) * 1024u + 16u * whalf;
;     const unsigned wper_dn = (unsigned)fwd_lane16(wcol) * 1024u + 16u * whalf;
;     auto w_store = [&](int j) __attribute__((always_inline)) { const float* src; unsigned char* dst; int ld, n0, k0; bool gu; w_decode(j, src, dst, ld, n0, k0, gu);
;         const int nb = n0 >> 8; const unsigned uni = (unsigned)(gu ? (nb & 3) * 512 + (nb >> 2) * 128 : nb * 256) * 1024u + (unsigned)k0;
;         const unsigned off = (gu ? wper_gu : wper_dn) + uni;
;         const unsigned* t = (const unsigned*)(lds + AT_WT + wcol * WPITCH + 16 * whalf);
;         *(u32x4*)(dst + off) = (u32x4){t[0], t[1], t[2], t[3]}; };
;     ...
;     auto step = [&](int t, u32x2& kl, u32x2& vl, const u32x2& ks, const u32x2& vs, f32x16& c0, f32x16& c1, f32x16& n0, f32x16& n1, const int hk, const int wj) __attribute__((always_inline)) {
;         const int slot1 = slot == 2 ? 0 : slot + 1, slot2 = slot1 == 2 ? 0 : slot1 + 1;
;         if (hk == 1) { w_cvt(); w_issue(wj + 1 < AT_NWT ? wj + 1 : AT_NWT - 1); }
;         if (hk == 2) w_store(wj);
;         { const int tn = t + 3; gload(tn < a.t1 ? tn : a.t1 - 1, kl, vl); }
;         const unsigned char* Kb = lds + slot * AT_BUFB; const unsigned char* Kn = lds + slot1 * AT_BUFB;
;         const v8i k0 = kread(Kn, 0), k1 = kread(Kn, 1), v0 = vread(Kb, 0), v1 = vread(Kb, 1);
;         n0 = mfma8(k0, qf8, cinit); n1 = mfma8(k1, qf8, cinit);
.LBB0_707:
	s_and_b32 s4, s15, 3
	s_add_i32 s4, s25, s4
	s_lshl_b32 s4, s4, 5
	s_add_i32 s4, s4, s16
	s_mul_hi_i32 s11, s8, s4
	s_mul_i32 s10, s8, s4
	s_lshl_b64 s[10:11], s[10:11], 2
	s_add_u32 s4, s6, s10
	s_addc_u32 s7, s7, s11
	s_lshl_b32 s6, s9, 2
	s_add_u32 s6, s4, s6
	s_addc_u32 s7, s7, 0
	s_cmp_lt_u32 s15, 12
	s_cbranch_scc1 .Lmy_a8l0
	s_load_dwordx2 s[6:7], s[0:1], 0xb0
	s_waitcnt lgkmcnt(0)
.Lmy_a8l0:
	v_lshl_add_u64 v[66:67], s[6:7], 0, v[106:107]
	s_lshl_b32 s4, s8, 2
	s_cmp_lt_u32 s15, 12
	s_cselect_b32 s4, s4, 0
	v_lshl_add_u64 v[74:75], v[66:67], 0, s[4:5]
	v_lshl_add_u64 v[76:77], v[74:75], 0, s[4:5]
	v_lshl_add_u64 v[78:79], v[76:77], 0, s[4:5]
	s_min_i32 s4, s56, 64
	s_cmp_lt_u32 s56, 61
	s_cselect_b64 s[8:9], -1, 0
	s_lshl_b32 s4, s4, 6
	s_add_i32 s12, s4, 0xc0
	s_add_i32 s13, s4, 0xfffff0c0
	s_and_b64 s[10:11], s[8:9], exec
	s_cselect_b32 s10, s12, s13
	s_add_i32 s11, s14, 1
	s_cmp_lg_u32 s14, 2
	s_cselect_b32 s25, s11, 0
	s_mul_i32 s11, s25, 0x4680
	v_add_u32_e32 v164, s11, v157
	ds_read_b128 v[66:69], v164
	ds_read_b128 v[70:73], v164 offset:16
	global_load_dwordx4 v[116:119], v106, s[6:7] nt
	global_load_dwordx4 v[112:115], v[74:75], off nt
	global_load_dwordx4 v[120:123], v[76:77], off nt
	global_load_dwordx4 v[124:127], v[78:79], off nt
	v_add_u32_e32 v74, s10, v154
	s_and_b64 s[6:7], s[8:9], exec
	v_ashrrev_i32_e32 v75, 31, v74
	s_cselect_b32 s6, s58, s60
	s_cselect_b32 s7, s59, s61
	v_lshlrev_b64 v[74:75], 7, v[74:75]
	v_lshl_add_u64 v[74:75], s[6:7], 0, v[74:75]
	v_lshl_add_u64 v[140:141], v[132:133], 0, s[4:5]
	s_mul_i32 s4, s14, 0x4680
	v_lshl_add_u64 v[74:75], v[74:75], 0, v[130:131]
	v_add_u32_e32 v165, s4, v157
	s_waitcnt lgkmcnt(0)
	v_mfma_f32_32x32x64_f8f6f4 v[82:97], v[66:73], v[98:105], 0
	ds_read_b128 v[66:69], v164 offset:2560
	ds_read_b128 v[70:73], v164 offset:2576
	global_load_dwordx2 v[138:139], v[74:75], off
	ds_read_b128 v[166:169], v165 offset:5120
	ds_read_b128 v[170:173], v165 offset:5136
	global_load_dwordx2 v[140:141], v[140:141], off offset:192
	v_exp_f32_e32 v150, v50
	v_exp_f32_e32 v151, v51
	v_exp_f32_e32 v146, v52
	v_exp_f32_e32 v147, v53
	v_exp_f32_e32 v142, v54
	v_exp_f32_e32 v143, v55
	v_exp_f32_e32 v148, v56
	v_exp_f32_e32 v149, v57
	v_exp_f32_e32 v144, v58
	v_exp_f32_e32 v145, v59
	v_exp_f32_e32 v52, v62
	v_exp_f32_e32 v53, v63
	v_exp_f32_e32 v56, v34
	v_exp_f32_e32 v57, v35
	v_exp_f32_e32 v38, v38
	v_exp_f32_e32 v39, v39
	v_exp_f32_e32 v42, v42
	v_exp_f32_e32 v43, v43
	v_exp_f32_e32 v34, v46
	v_exp_f32_e32 v35, v47
	v_exp_f32_e32 v58, v60
	v_exp_f32_e32 v59, v61
	v_exp_f32_e32 v60, v64
	v_exp_f32_e32 v61, v65
	v_exp_f32_e32 v50, v36
	v_exp_f32_e32 v51, v37
	v_exp_f32_e32 v54, v40
	v_exp_f32_e32 v55, v41
	v_exp_f32_e32 v36, v44
	v_exp_f32_e32 v37, v45
	v_exp_f32_e32 v40, v48
	v_exp_f32_e32 v41, v49
	s_nop 0
	s_nop 0
	s_nop 0
	s_nop 0
	s_nop 0
	s_nop 0
	s_nop 0
	s_nop 0
	v_cvt_scalef32_pk_fp8_f32 v174, v150, v151, s48
	v_cvt_scalef32_pk_fp8_f32 v178, v56, v57, s48
	v_cvt_scalef32_pk_fp8_f32 v175, v142, v143, s48
	v_cvt_scalef32_pk_fp8_f32 v179, v38, v39, s48
	v_cvt_scalef32_pk_fp8_f32 v176, v144, v145, s48
	v_cvt_scalef32_pk_fp8_f32 v180, v42, v43, s48
	v_cvt_scalef32_pk_fp8_f32 v177, v52, v53, s48
	v_cvt_scalef32_pk_fp8_f32 v181, v34, v35, s48
	v_cvt_scalef32_pk_fp8_f32 v174, v146, v147, s48 op_sel:[0,0,0,1]
	v_cvt_scalef32_pk_fp8_f32 v178, v50, v51, s48 op_sel:[0,0,0,1]
	v_cvt_scalef32_pk_fp8_f32 v175, v148, v149, s48 op_sel:[0,0,0,1]
	v_cvt_scalef32_pk_fp8_f32 v179, v54, v55, s48 op_sel:[0,0,0,1]
	v_cvt_scalef32_pk_fp8_f32 v176, v58, v59, s48 op_sel:[0,0,0,1]
	v_cvt_scalef32_pk_fp8_f32 v180, v36, v37, s48 op_sel:[0,0,0,1]
	v_cvt_scalef32_pk_fp8_f32 v177, v60, v61, s48 op_sel:[0,0,0,1]
	v_cvt_scalef32_pk_fp8_f32 v181, v40, v41, s48 op_sel:[0,0,0,1]
	s_addk_i32 s11, 0x4680
	s_cmp_eq_u32 s25, 2
	s_waitcnt lgkmcnt(0)
	v_mfma_f32_32x32x64_f8f6f4 v[18:33], v[166:173], v[174:181], v[18:33]
	ds_read_b128 v[166:169], v165 offset:7680
	ds_read_b128 v[170:173], v165 offset:7696
	s_cselect_b64 s[6:7], -1, 0
	s_and_b64 s[8:9], s[6:7], exec
	s_cselect_b32 s4, 0, s11
	s_add_i32 s4, s4, 0
	v_add_u32_e32 v44, s4, v155
	s_waitcnt vmcnt(7)
	ds_write_b64 v44, v[134:135]
	v_add_u32_e32 v44, s4, v156
	s_and_b32 s4, s19, 0xe00
	s_add_i32 s8, s4, s62
	s_mul_hi_u32 s4, s8, 0xaaaaaaab
	s_lshr_b32 s4, s4, 6
	s_mul_i32 s65, s4, 0xffffffa0
	v_add_u32_e32 v44, 0x1400, v44
	s_add_i32 s65, s65, s8
	v_mfma_f32_32x32x64_f8f6f4 v[66:81], v[66:73], v[98:105], 0
	s_mov_b64 s[8:9], s[0:1]
	s_waitcnt vmcnt(6)
	ds_write2_b32 v44, v136, v137 offset1:8
	s_waitcnt lgkmcnt(0)
	s_barrier
	s_load_dwordx2 s[12:13], s[8:9], 0xd8
	s_cmp_lt_i32 s65, 64
	s_cselect_b64 s[10:11], -1, 0
	s_cmp_gt_i32 s65, 63
	s_mov_b64 s[14:15], -1
	v_mfma_f32_32x32x64_f8f6f4 v[2:17], v[166:173], v[174:181], v[2:17]
	s_cbranch_scc0 .LBB0_709
	s_lshl_b64 s[8:9], s[4:5], 20
	s_waitcnt lgkmcnt(0)
	s_add_u32 s8, s12, s8
	s_addc_u32 s9, s13, s9
	s_add_u32 s8, s8, 0x11094000
	s_addc_u32 s9, s9, 0
	s_cmp_lt_u32 s24, 12
	s_cbranch_scc1 .Lmy_a8s0d
	s_add_u32 s8, s12, 0x1c094000
	s_addc_u32 s9, s13, 0
.Lmy_a8s0d:
	s_and_b32 s14, s65, 0x7ffffffc
	s_sub_i32 s63, s14, 64
	s_mov_b64 s[14:15], 0
.LBB0_709:
	s_andn2_b64 vcc, exec, s[14:15]
	v_mov_b32_e32 v44, v161
	s_mov_b32 s14, s17
	s_cbranch_vccnz .LBB0_702
	s_lshl_b64 s[8:9], s[4:5], 21
	s_waitcnt lgkmcnt(0)
	s_add_u32 s4, s12, s8
	s_addc_u32 s9, s13, s9
	s_add_u32 s8, s4, 0x1094000
	s_addc_u32 s9, s9, 0
	s_cmp_lt_u32 s24, 12
	s_cbranch_scc1 .Lmy_a8s0g
	s_add_u32 s8, s12, 0x1c094000
	s_addc_u32 s9, s13, 0
.Lmy_a8s0g:
	s_ashr_i32 s4, s65, 1
	s_and_b32 s63, s4, -4
	v_mov_b32_e32 v44, v159
	s_mov_b32 s14, s18
	s_branch .LBB0_702

; DI f32x16 mfma8(v8i a, v8i b, f32x16 c) { return __builtin_amdgcn_mfma_scale_f32_32x32x64_f8f6f4(a, b, c, 0, 0, 0, 0, 0, 0); }
; DI void attn_unit_d8(unsigned char* lds, const AttnArgs& a) {
;     ...
;     auto tile = [&](const unsigned char* Kb, const unsigned char* Kn, v8i& Pa, v8i& Pb, v8i& v0, v8i& v1, const v8i& Qa, const v8i& Qb, const v8i& w0, const v8i& w1) __attribute__((always_inline)) {
;         qk(Kb, 1, s1a, s1b);
;         v0 = rd32(Kb + voff); v1 = rd32(Kb + voff + 32 * A8_PITCH);
;         o0[0] = mfma8(w0, Qa, o0[0]); o1[0] = mfma8(w0, Qb, o1[0]); o0[1] = mfma8(w1, Qa, o0[1]); o1[1] = mfma8(w1, Qb, o1[1]);
;         expsum(s0a, l0); expsum(s0b, l1); pack4(s0a, Pa, 0); pack4(s0b, Pb, 0);
;         qk(Kn, 0, s0a, s0b);
;         expsum(s1a, l0); expsum(s1b, l1); pack4(s1a, Pa, 4); pack4(s1b, Pb, 4);
; #pragma unroll
;         for (int i = 0; i < 8; ++i) { __builtin_amdgcn_sched_group_barrier(0x008, 1, 0); __builtin_amdgcn_sched_group_barrier(0x402, 22, 0); }
;     };
;     for (int t = a.t0; t < a.t1; t += 2) {
;         const int s1 = sb + 1 >= 5 ? sb - 4 : sb + 1, s2 = sb + 2 >= 5 ? sb - 3 : sb + 2, s3 = sb + 3 >= 5 ? sb - 2 : sb + 3, s4 = sb + 4 >= 5 ? sb - 1 : sb + 4;
;         { const int ta = t + 3, tb = t + 4; gload(ta < a.t1 ? ta : a.t1 - 1, kreg0, vreg0); gload(tb < a.t1 ? tb : a.t1 - 1, kreg1, vreg1); }
;         tile(lds + sb * D8_SLOT, lds + s1 * D8_SLOT, PaX, PbX, vX0, vX1, PaY, PbY, vY0, vY1);
.LBB0_1888:
	s_add_i32 s22, s22, 2
	s_mul_i32 s8, s23, 0x2800
	s_cmp_gt_i32 s23, 3
	v_mfma_f32_32x32x64_f8f6f4 v[50:65], v[154:161], v[138:145], v[50:65]
	v_exp_f32_e32 v194, v90
	v_add_u32_e32 v90, s8, v219
	s_cselect_b32 s8, -4, 1
	s_add_i32 s51, s8, s23
	s_cmp_gt_i32 s23, 2
	s_cselect_b32 s8, -3, 2
	s_add_i32 s8, s8, s23
	s_cmp_gt_i32 s23, 1
	s_cselect_b32 s52, -2, 3
	s_add_i32 s52, s52, s23
	s_cmp_gt_i32 s23, 0
	s_cselect_b32 s53, -1, 4
	s_min_u32 s56, s22, 64
	s_add_i32 s53, s53, s23
	s_cmp_lt_u32 s22, 61
	s_mul_i32 s50, s8, 0x2800
	s_mov_b32 s23, s8
	s_cselect_b64 s[54:55], -1, 0
	s_lshl_b32 s8, s56, 6
	s_add_i32 s56, s8, 0xc0
	s_add_i32 s57, s8, 0xfffff0c0
	s_and_b64 s[54:55], s[54:55], exec
	v_lshl_add_u64 v[98:99], v[184:185], 0, s[8:9]
	s_cselect_b32 s8, s56, s57
	s_cselect_b32 s55, s19, s21
	s_cselect_b32 s54, s18, s20
	s_min_u32 s58, s22, 63
	v_exp_f32_e32 v200, v82
	v_exp_f32_e32 v201, v83
	v_exp_f32_e32 v198, v84
	v_exp_f32_e32 v199, v85
	v_exp_f32_e32 v202, v86
	v_exp_f32_e32 v203, v87
	v_exp_f32_e32 v196, v88
	v_exp_f32_e32 v197, v89
	ds_read_b128 v[82:85], v90 offset:2560
	ds_read_b128 v[86:89], v90 offset:2576
	global_load_dwordx2 v[204:205], v[98:99], off offset:192
	v_add_u32_e32 v98, s8, v182
	s_cmp_lt_u32 s22, 60
	v_ashrrev_i32_e32 v99, 31, v98
	s_cselect_b64 s[56:57], -1, 0
	s_lshl_b32 s8, s58, 6
	v_lshlrev_b64 v[98:99], 8, v[98:99]
	s_add_i32 s58, s8, 0x100
	s_add_i32 s59, s8, 0xfffff100
	v_lshl_add_u64 v[98:99], s[54:55], 0, v[98:99]
	s_and_b64 s[54:55], s[56:57], exec
	v_lshl_add_u64 v[100:101], v[184:185], 0, s[8:9]
	s_cselect_b32 s8, s58, s59
	v_lshl_add_u64 v[220:221], v[98:99], 0, v[178:179]
	v_add_u32_e32 v98, s8, v182
	v_ashrrev_i32_e32 v99, 31, v98
	s_cselect_b32 s55, s19, s21
	s_cselect_b32 s54, s18, s20
	v_lshlrev_b64 v[98:99], 8, v[98:99]
	v_lshl_add_u64 v[98:99], s[54:55], 0, v[98:99]
	global_load_dwordx2 v[206:207], v[100:101], off offset:256
	v_lshl_add_u64 v[222:223], v[98:99], 0, v[178:179]
	s_waitcnt lgkmcnt(0)
	v_mfma_f32_32x32x64_f8f6f4 v[98:113], v[82:89], v[114:121], 0
	v_exp_f32_e32 v195, v91
	v_exp_f32_e32 v224, v92
	v_exp_f32_e32 v225, v93
	v_exp_f32_e32 v226, v94
	v_exp_f32_e32 v227, v95
	v_exp_f32_e32 v228, v96
	v_exp_f32_e32 v229, v97
	ds_read_b128 v[170:173], v90 offset:5120
	ds_read_b128 v[174:177], v90 offset:5136
	ds_read_b128 v[162:165], v90 offset:7680
	ds_read_b128 v[166:169], v90 offset:7696
	v_pk_add_f32 v[90:91], v[188:189], v[200:201]
	v_pk_add_f32 v[92:93], v[186:187], v[198:199]
	v_pk_add_f32 v[90:91], v[202:203], v[90:91]
	v_pk_add_f32 v[92:93], v[196:197], v[92:93]
	v_pk_add_f32 v[90:91], v[194:195], v[90:91]
	v_pk_add_f32 v[92:93], v[224:225], v[92:93]
	v_exp_f32_e32 v66, v66
	v_exp_f32_e32 v67, v67
	v_exp_f32_e32 v68, v68
	v_exp_f32_e32 v69, v69
	v_exp_f32_e32 v70, v70
	v_exp_f32_e32 v71, v71
	v_exp_f32_e32 v72, v72
	v_pk_add_f32 v[230:231], v[228:229], v[92:93]
	v_pk_add_f32 v[232:233], v[226:227], v[90:91]
	v_mfma_f32_32x32x64_f8f6f4 v[82:97], v[82:89], v[122:129], 0
	v_exp_f32_e32 v73, v73
	v_exp_f32_e32 v74, v74
	v_exp_f32_e32 v75, v75
	v_exp_f32_e32 v76, v76
	v_exp_f32_e32 v77, v77
	v_exp_f32_e32 v78, v78
	v_exp_f32_e32 v79, v79
	v_exp_f32_e32 v80, v80
	v_exp_f32_e32 v81, v81
	v_pk_add_f32 v[188:189], v[192:193], v[66:67]
	v_pk_add_f32 v[190:191], v[190:191], v[68:69]
	s_nop 0
	v_pk_add_f32 v[188:189], v[70:71], v[188:189]
	v_pk_add_f32 v[190:191], v[72:73], v[190:191]
	s_nop 0
	v_cvt_scalef32_pk_fp8_f32 v186, v200, v201, s36
	v_pk_add_f32 v[188:189], v[74:75], v[188:189]
	v_pk_add_f32 v[190:191], v[76:77], v[190:191]
	v_cvt_scalef32_pk_fp8_f32 v187, v202, v203, s36
	v_cvt_scalef32_pk_fp8_f32 v186, v198, v199, s36 op_sel:[0,0,0,1]
	v_pk_add_f32 v[192:193], v[78:79], v[188:189]
	v_pk_add_f32 v[190:191], v[80:81], v[190:191]
	v_mfma_f32_32x32x64_f8f6f4 v[2:17], v[154:161], v[130:137], v[2:17]
	s_nop 0
	s_nop 0
	s_nop 0
	s_nop 0
	s_nop 0
	s_nop 0
	s_mulk_i32 s51, 0x2800
	v_cvt_scalef32_pk_fp8_f32 v188, v194, v195, s36
	v_cvt_scalef32_pk_fp8_f32 v189, v226, v227, s36
	v_cvt_scalef32_pk_fp8_f32 v154, v66, v67, s36
	v_cvt_scalef32_pk_fp8_f32 v155, v70, v71, s36
	v_cvt_scalef32_pk_fp8_f32 v156, v74, v75, s36
	v_cvt_scalef32_pk_fp8_f32 v157, v78, v79, s36
	v_cvt_scalef32_pk_fp8_f32 v187, v196, v197, s36 op_sel:[0,0,0,1]
	v_add_u32_e32 v234, s51, v219
	v_cvt_scalef32_pk_fp8_f32 v188, v224, v225, s36 op_sel:[0,0,0,1]
	v_cvt_scalef32_pk_fp8_f32 v189, v228, v229, s36 op_sel:[0,0,0,1]
	v_cvt_scalef32_pk_fp8_f32 v154, v68, v69, s36 op_sel:[0,0,0,1]
	v_cvt_scalef32_pk_fp8_f32 v155, v72, v73, s36 op_sel:[0,0,0,1]
	v_cvt_scalef32_pk_fp8_f32 v156, v76, v77, s36 op_sel:[0,0,0,1]
	v_cvt_scalef32_pk_fp8_f32 v157, v80, v81, s36 op_sel:[0,0,0,1]
	v_exp_f32_e32 v98, v98
	v_exp_f32_e32 v99, v99
	v_mfma_f32_32x32x64_f8f6f4 v[34:49], v[146:153], v[138:145], v[34:49]
	v_exp_f32_e32 v100, v100
	v_exp_f32_e32 v101, v101
	v_exp_f32_e32 v102, v102
	v_exp_f32_e32 v103, v103
	v_exp_f32_e32 v104, v104
	v_exp_f32_e32 v105, v105
	v_exp_f32_e32 v106, v106
	v_exp_f32_e32 v107, v107
	v_exp_f32_e32 v108, v108
	v_exp_f32_e32 v109, v109
	v_exp_f32_e32 v110, v110
	v_exp_f32_e32 v111, v111
	v_exp_f32_e32 v112, v112
	v_exp_f32_e32 v113, v113
	ds_read_b128 v[194:197], v234
	ds_read_b128 v[198:201], v234 offset:16
	v_pk_add_f32 v[66:67], v[232:233], v[98:99]
	v_pk_add_f32 v[68:69], v[230:231], v[100:101]
	v_pk_add_f32 v[66:67], v[102:103], v[66:67]
	v_pk_add_f32 v[68:69], v[104:105], v[68:69]
	v_pk_add_f32 v[66:67], v[106:107], v[66:67]
	v_pk_add_f32 v[68:69], v[108:109], v[68:69]
	v_pk_add_f32 v[140:141], v[110:111], v[66:67]
	v_pk_add_f32 v[138:139], v[112:113], v[68:69]
	v_mfma_f32_32x32x64_f8f6f4 v[18:33], v[146:153], v[130:137], v[18:33]
	v_exp_f32_e32 v82, v82
	v_exp_f32_e32 v83, v83
	v_exp_f32_e32 v84, v84
	v_exp_f32_e32 v85, v85
	v_exp_f32_e32 v86, v86
	v_exp_f32_e32 v87, v87
	v_exp_f32_e32 v88, v88
	v_exp_f32_e32 v89, v89
	v_exp_f32_e32 v90, v90
	v_exp_f32_e32 v91, v91
	v_exp_f32_e32 v92, v92
	v_exp_f32_e32 v93, v93
	v_exp_f32_e32 v94, v94
	v_exp_f32_e32 v95, v95
	v_exp_f32_e32 v96, v96
	v_exp_f32_e32 v97, v97
	v_pk_add_f32 v[66:67], v[192:193], v[82:83]
	v_pk_add_f32 v[68:69], v[190:191], v[84:85]
	v_pk_add_f32 v[66:67], v[86:87], v[66:67]
	v_pk_add_f32 v[68:69], v[88:89], v[68:69]
	v_pk_add_f32 v[130:131], v[90:91], v[66:67]
	v_pk_add_f32 v[132:133], v[92:93], v[68:69]
	s_waitcnt lgkmcnt(0)
; DI KParamsPtr kparams() { KParamsPtr p = (KParamsPtr)__builtin_amdgcn_kernarg_segment_ptr(); asm volatile("" : "+s"(p)); return p; }
; DI void attn_unit_a8(unsigned char* lds, const AttnArgs& a) {
;     ...
;     auto w_decode = [&](int j, const float*& src, unsigned char*& dst, int& ld, int& n0, int& k0, bool& gu) __attribute__((always_inline)) {
;         const int g = (j >> 2) * 512 + a.wl, e = g / 96, rr = g - e * 96; KParamsPtr kp = kparams();
;         if (rr < 64) { src = kp->w_gu + ((size_t)a.wli * NE + e) * (1024 * 2048); dst = kp->ws + WS_WGU + (size_t)a.wli * SZ_WGU + (size_t)e * 2048 * 1024; ld = 2048; n0 = (rr & 7) * 256; k0 = ((rr >> 3) * 4 + (j & 3)) * 32; gu = true; }
;         else { const int q = rr - 64; src = kp->w_dn + ((size_t)a.wli * NE + e) * (1024 * 1024); dst = kp->ws + WS_WDN + (size_t)a.wli * SZ_WDN + (size_t)e * 1024 * 1024; ld = 1024; n0 = (q & 3) * 256; k0 = ((q >> 2) * 4 + (j & 3)) * 32; gu = false; } };
;     auto w_issue = [&](int j) __attribute__((always_inline)) { const float* src; unsigned char* dst; int ld, n0, k0; bool gu; w_decode(j, src, dst, ld, n0, k0, gu);
;         const float* p = src + (size_t)(k0 + 4 * wid) * ld + n0 + wn4;
;         wq[0] = __builtin_nontemporal_load((const f32x4*)p); wq[1] = __builtin_nontemporal_load((const f32x4*)(p + ld));
;         wq[2] = __builtin_nontemporal_load((const f32x4*)(p + (size_t)2 * ld)); wq[3] = __builtin_nontemporal_load((const f32x4*)(p + (size_t)3 * ld)); };
; DI void attn_unit_d8(unsigned char* lds, const AttnArgs& a) {
;     ...
;     auto tile = [&](const unsigned char* Kb, const unsigned char* Kn, v8i& Pa, v8i& Pb, v8i& v0, v8i& v1, const v8i& Qa, const v8i& Qb, const v8i& w0, const v8i& w1) __attribute__((always_inline)) {
;         qk(Kb, 1, s1a, s1b);
;         v0 = rd32(Kb + voff); v1 = rd32(Kb + voff + 32 * A8_PITCH);
;         o0[0] = mfma8(w0, Qa, o0[0]); o1[0] = mfma8(w0, Qb, o1[0]); o0[1] = mfma8(w1, Qa, o0[1]); o1[1] = mfma8(w1, Qb, o1[1]);
;         expsum(s0a, l0); expsum(s0b, l1); pack4(s0a, Pa, 0); pack4(s0b, Pb, 0);
;         qk(Kn, 0, s0a, s0b);
;         expsum(s1a, l0); expsum(s1b, l1); pack4(s1a, Pa, 4); pack4(s1b, Pb, 4);
; #pragma unroll
;         for (int i = 0; i < 8; ++i) { __builtin_amdgcn_sched_group_barrier(0x008, 1, 0); __builtin_amdgcn_sched_group_barrier(0x402, 22, 0); }
;     };
	v_mfma_f32_32x32x64_f8f6f4 v[66:81], v[194:201], v[114:121], 0
	s_nop 0
	s_nop 0
	s_nop 0
	s_nop 0
	s_nop 0
	s_nop 0
	s_nop 0
	v_cvt_scalef32_pk_fp8_f32 v190, v98, v99, s36
	v_cvt_scalef32_pk_fp8_f32 v191, v102, v103, s36
	v_cvt_scalef32_pk_fp8_f32 v192, v106, v107, s36
	v_cvt_scalef32_pk_fp8_f32 v193, v110, v111, s36
	v_cvt_scalef32_pk_fp8_f32 v158, v82, v83, s36
	v_cvt_scalef32_pk_fp8_f32 v159, v86, v87, s36
	v_pk_add_f32 v[142:143], v[96:97], v[132:133]
	v_pk_add_f32 v[144:145], v[94:95], v[130:131]
	v_cvt_scalef32_pk_fp8_f32 v160, v90, v91, s36
	v_cvt_scalef32_pk_fp8_f32 v190, v100, v101, s36 op_sel:[0,0,0,1]
	v_cvt_scalef32_pk_fp8_f32 v191, v104, v105, s36 op_sel:[0,0,0,1]
	v_cvt_scalef32_pk_fp8_f32 v192, v108, v109, s36 op_sel:[0,0,0,1]
	v_cvt_scalef32_pk_fp8_f32 v193, v112, v113, s36 op_sel:[0,0,0,1]
	v_cvt_scalef32_pk_fp8_f32 v158, v84, v85, s36 op_sel:[0,0,0,1]
	v_cvt_scalef32_pk_fp8_f32 v159, v88, v89, s36 op_sel:[0,0,0,1]
	v_mfma_f32_32x32x64_f8f6f4 v[98:113], v[194:201], v[122:129], 0
	global_load_dwordx2 v[194:195], v[220:221], off
	global_load_dwordx2 v[196:197], v[222:223], off
	ds_read_b128 v[130:133], v234 offset:2560
	ds_read_b128 v[134:137], v234 offset:2576
	v_exp_f32_e32 v146, v66
	s_add_i32 s80, s61, 12
	v_exp_f32_e32 v147, v67
	s_lshr_b32 s73, s80, 2
	s_mulk_i32 s52, 0x2800
	s_nop 0
	s_add_i32 s8, s52, 0
	v_cvt_scalef32_pk_fp8_f32 v161, v94, v95, s36
	v_add_u32_e32 v224, s8, v183
	v_cvt_scalef32_pk_fp8_f32 v160, v92, v93, s36 op_sel:[0,0,0,1]
	v_cvt_scalef32_pk_fp8_f32 v161, v96, v97, s36 op_sel:[0,0,0,1]
	v_exp_f32_e32 v148, v68
	s_lshl_b32 s73, s73, 9
	v_exp_f32_e32 v149, v69
	s_add_i32 s73, s73, s46
	v_exp_f32_e32 v150, v70
	s_mul_i32 s75, s73, 0xaaab
	v_exp_f32_e32 v151, v71
	s_lshr_b32 s75, s75, 22
	v_exp_f32_e32 v152, v72
	s_mul_i32 s76, s75, 0x60
	v_exp_f32_e32 v153, v73
	s_sub_i32 s76, s73, s76
	v_exp_f32_e32 v198, v74
	s_lshr_b32 s77, s76, 6
	v_exp_f32_e32 v199, v75
	s_lshl_b32 s78, s77, 6
	v_exp_f32_e32 v200, v76
	s_sub_i32 s76, s76, s78
	v_exp_f32_e32 v201, v77
	s_sub_i32 s78, 3, s77
	v_exp_f32_e32 v202, v78
	s_lshr_b32 s79, s76, s78
	v_exp_f32_e32 v203, v79
	s_lshl_b32 s79, s79, 2
	v_exp_f32_e32 v220, v80
	s_and_b32 s81, s80, 3
	v_exp_f32_e32 v221, v81
	s_add_i32 s79, s79, s81
	v_pk_add_f32 v[66:67], v[140:141], v[146:147]
	s_waitcnt lgkmcnt(0)
	v_mfma_f32_32x32x64_f8f6f4 v[82:97], v[130:137], v[114:121], 0
	v_add_f32_e64 v68, v138, v148
	v_add_f32_e64 v69, v139, v149
	v_add_f32_e64 v66, v150, v66
	v_add_f32_e64 v67, v151, v67
	v_add_f32_e64 v68, v152, v68
	v_add_f32_e64 v69, v153, v69
	v_add_f32_e64 v138, v198, v66
	v_add_f32_e64 v139, v199, v67
	v_add_f32_e64 v140, v200, v68
	v_add_f32_e64 v141, v201, v69
	v_exp_f32_e32 v98, v98
	s_lshl_b32 s79, s79, 5
	v_exp_f32_e32 v99, v99
	s_lshl_b32 s81, s63, 2
	v_exp_f32_e32 v100, v100
	s_add_i32 s81, s81, s79
	v_exp_f32_e32 v101, v101
	s_sub_i32 s78, 13, s77
	v_exp_f32_e32 v102, v102
	s_lshl_b32 s81, s81, s78
	v_exp_f32_e32 v103, v103
	s_lshr_b32 s78, 7, s77
	v_exp_f32_e32 v104, v104
	s_and_b32 s78, s76, s78
	v_exp_f32_e32 v105, v105
	s_lshl_b32 s72, s78, 10
	v_exp_f32_e32 v106, v106
	s_add_i32 s81, s81, s72
	v_exp_f32_e32 v107, v107
	s_add_i32 s72, s75, 32
	v_exp_f32_e32 v108, v108
	s_sub_i32 s80, 23, s77
	v_exp_f32_e32 v109, v109
	s_lshl_b32 s72, s72, s80
	v_exp_f32_e32 v110, v110
	s_add_i32 s81, s81, s72
	v_exp_f32_e32 v111, v111
	s_cmp_eq_u32 s77, 0
	s_cselect_b64 s[84:85], s[66:67], s[68:69]
	v_exp_f32_e32 v112, v112
	s_add_u32 s84, s84, s81
	s_addc_u32 s85, s85, 0
	v_exp_f32_e32 v113, v113
	s_lshr_b32 s80, 0x2000, s77
	v_exp_f32_e32 v82, v82
	s_and_b32 s72, s78, 3
	v_mfma_f32_32x32x64_f8f6f4 v[66:81], v[130:137], v[122:129], 0
	v_add_f32_e64 v130, v144, v98
	v_add_f32_e64 v131, v145, v99
	v_add_f32_e64 v132, v142, v100
	v_add_f32_e64 v133, v143, v101
	v_add_f32_e64 v142, v102, v130
	v_add_f32_e64 v143, v103, v131
	v_add_f32_e64 v132, v104, v132
	v_add_f32_e64 v133, v105, v133
	v_add_f32_e64 v134, v220, v140
	v_add_f32_e64 v135, v221, v141
	v_add_f32_e64 v136, v202, v138
	v_add_f32_e64 v137, v203, v139
	s_nop 0
	s_nop 0
	s_nop 0
	s_nop 0
	s_nop 0
	s_nop 0
	v_pk_add_f32 v[142:143], v[106:107], v[142:143]
	v_pk_add_f32 v[132:133], v[108:109], v[132:133]
	v_cvt_scalef32_pk_fp8_f32 v138, v146, v147, s36
	v_cvt_scalef32_pk_fp8_f32 v139, v150, v151, s36
	v_cvt_scalef32_pk_fp8_f32 v140, v198, v199, s36
	v_cvt_scalef32_pk_fp8_f32 v141, v202, v203, s36
	v_cvt_scalef32_pk_fp8_f32 v130, v98, v99, s36
	v_cvt_scalef32_pk_fp8_f32 v131, v102, v103, s36
	v_pk_add_f32 v[146:147], v[112:113], v[132:133]
	v_pk_add_f32 v[150:151], v[110:111], v[142:143]
	v_mfma_f32_32x32x64_f8f6f4 v[50:65], v[170:177], v[186:193], v[50:65]
	v_exp_f32_e32 v83, v83
	s_lshl_b32 s72, s72, 19
	v_exp_f32_e32 v84, v84
	s_lshr_b32 s81, s78, 2
	v_exp_f32_e32 v85, v85
; DI unsigned pk4_fp8_mul64(float a, float b, float c, float d) { v2s_t r = {0, 0}; r = __builtin_amdgcn_cvt_scalef32_pk_fp8_f32(r, a, b, 0.015625f, false); r = __builtin_amdgcn_cvt_scalef32_pk_fp8_f32(r, c, d, 0.015625f, true); return __builtin_bit_cast(unsigned, r); }
; DI f32x16 mfma8(v8i a, v8i b, f32x16 c) { return __builtin_amdgcn_mfma_scale_f32_32x32x64_f8f6f4(a, b, c, 0, 0, 0, 0, 0, 0); }
; DI void attn_unit_a8(unsigned char* lds, const AttnArgs& a) {
;     ...
;     auto w_cvt = [&]() __attribute__((always_inline)) { unsigned char* t8 = lds + AT_WT + wn4 * WPITCH + 4 * wid;
; #pragma unroll
;         for (int j = 0; j < 4; ++j) *(unsigned*)(t8 + j * WPITCH) = pk4_fp8_mul64(wq[0][j], wq[1][j], wq[2][j], wq[3][j]); };
; DI void attn_unit_d8(unsigned char* lds, const AttnArgs& a) {
;     ...
;     auto tile = [&](const unsigned char* Kb, const unsigned char* Kn, v8i& Pa, v8i& Pb, v8i& v0, v8i& v1, const v8i& Qa, const v8i& Qb, const v8i& w0, const v8i& w1) __attribute__((always_inline)) {
;         qk(Kb, 1, s1a, s1b);
;         v0 = rd32(Kb + voff); v1 = rd32(Kb + voff + 32 * A8_PITCH);
;         o0[0] = mfma8(w0, Qa, o0[0]); o1[0] = mfma8(w0, Qb, o1[0]); o0[1] = mfma8(w1, Qa, o0[1]); o1[1] = mfma8(w1, Qb, o1[1]);
;         expsum(s0a, l0); expsum(s0b, l1); pack4(s0a, Pa, 0); pack4(s0b, Pb, 0);
;         qk(Kn, 0, s0a, s0b);
;         expsum(s1a, l0); expsum(s1b, l1); pack4(s1a, Pa, 4); pack4(s1b, Pb, 4);
; #pragma unroll
;         for (int i = 0; i < 8; ++i) { __builtin_amdgcn_sched_group_barrier(0x008, 1, 0); __builtin_amdgcn_sched_group_barrier(0x402, 22, 0); }
;     };
	s_lshl_b32 s81, s81, 17
	v_add_u32_e32 v102, s50, v219
	v_exp_f32_e32 v86, v86
	s_add_i32 s72, s72, s81
	v_exp_f32_e32 v87, v87
	s_lshl_b32 s81, s78, 18
	v_exp_f32_e32 v88, v88
	s_cmp_eq_u32 s77, 0
	s_cselect_b32 s72, s72, s81
	v_exp_f32_e32 v89, v89
	s_mul_i32 s81, s77, 0xc000000
	v_cvt_scalef32_pk_fp8_f32 v130, v100, v101, s36 op_sel:[0,0,0,1]
	v_cvt_scalef32_pk_fp8_f32 v131, v104, v105, s36 op_sel:[0,0,0,1]
	v_exp_f32_e32 v90, v90
	s_add_i32 s81, s81, 0x9094000
	v_exp_f32_e32 v91, v91
	s_add_i32 s72, s72, s79
	v_exp_f32_e32 v92, v92
	s_sub_i32 s73, 21, s77
	v_exp_f32_e32 v93, v93
	s_lshl_b32 s73, s75, s73
	ds_read_b128 v[98:101], v102
	ds_read_b128 v[102:105], v102 offset:16
	s_nop 0
	v_cvt_scalef32_pk_fp8_f32 v138, v148, v149, s36 op_sel:[0,0,0,1]
	v_cvt_scalef32_pk_fp8_f32 v139, v152, v153, s36 op_sel:[0,0,0,1]
	v_cvt_scalef32_pk_fp8_f32 v140, v200, v201, s36 op_sel:[0,0,0,1]
	v_cvt_scalef32_pk_fp8_f32 v141, v220, v221, s36 op_sel:[0,0,0,1]
	s_nop 0
	v_exp_f32_e32 v94, v94
	s_add_i32 s72, s72, s73
	v_exp_f32_e32 v95, v95
	s_add_u32 s72, s72, s81
	v_mfma_f32_32x32x64_f8f6f4 v[2:17], v[170:177], v[154:161], v[2:17]
	v_exp_f32_e32 v148, v96
	s_or_b32 s79, s72, s77
	v_cvt_scalef32_pk_fp8_f32 v132, v106, v107, s36
	v_exp_f32_e32 v149, v97
	v_pk_add_f32 v[96:97], v[136:137], v[82:83]
	v_pk_add_f32 v[106:107], v[134:135], v[84:85]
	v_exp_f32_e32 v66, v66
	v_exp_f32_e32 v67, v67
	v_exp_f32_e32 v68, v68
	v_exp_f32_e32 v69, v69
	v_cvt_scalef32_pk_fp8_f32 v133, v110, v111, s36
	v_pk_add_f32 v[106:107], v[88:89], v[106:107]
	v_pk_add_f32 v[96:97], v[86:87], v[96:97]
	v_exp_f32_e32 v70, v70
	v_exp_f32_e32 v71, v71
	v_exp_f32_e32 v72, v72
	v_exp_f32_e32 v73, v73
	v_cvt_scalef32_pk_fp8_f32 v132, v108, v109, s36 op_sel:[0,0,0,1]
	v_cvt_scalef32_pk_fp8_f32 v133, v112, v113, s36 op_sel:[0,0,0,1]
	v_pk_add_f32 v[96:97], v[90:91], v[96:97]
	v_pk_add_f32 v[106:107], v[92:93], v[106:107]
	v_exp_f32_e32 v74, v74
	v_exp_f32_e32 v75, v75
	v_mfma_f32_32x32x64_f8f6f4 v[34:49], v[162:169], v[186:193], v[34:49]
	v_exp_f32_e32 v76, v76
	v_exp_f32_e32 v77, v77
	v_exp_f32_e32 v78, v78
	v_exp_f32_e32 v79, v79
	s_nop 0
	v_exp_f32_e32 v80, v80
	v_exp_f32_e32 v81, v81
	s_nop 0
	s_nop 0
	v_cvt_scalef32_pk_fp8_f32 v142, v82, v83, s36
	s_nop 0
	v_cvt_scalef32_pk_fp8_f32 v143, v86, v87, s36
	v_cvt_scalef32_pk_fp8_f32 v144, v90, v91, s36
	v_cvt_scalef32_pk_fp8_f32 v142, v84, v85, s36 op_sel:[0,0,0,1]
	v_pk_add_f32 v[82:83], v[150:151], v[66:67]
	v_pk_add_f32 v[84:85], v[146:147], v[68:69]
	s_mulk_i32 s53, 0x2800
	v_pk_add_f32 v[186:187], v[148:149], v[106:107]
	v_pk_add_f32 v[188:189], v[94:95], v[96:97]
	v_cvt_scalef32_pk_fp8_f32 v145, v94, v95, s36
	v_cvt_scalef32_pk_fp8_f32 v143, v88, v89, s36 op_sel:[0,0,0,1]
	v_cvt_scalef32_pk_fp8_f32 v144, v92, v93, s36 op_sel:[0,0,0,1]
	v_pk_add_f32 v[84:85], v[72:73], v[84:85]
	v_mfma_f32_32x32x64_f8f6f4 v[18:33], v[162:169], v[154:161], v[18:33]
	v_add_f32_e64 v82, v70, v82
	v_add_f32_e64 v83, v71, v83
	s_nop 0
	s_nop 0
	s_nop 0
	s_nop 0
	s_add_i32 s51, s53, 0
	v_add_f32_e64 v82, v74, v82
	v_add_f32_e64 v83, v75, v83
	v_add_f32_e64 v84, v76, v84
	v_add_f32_e64 v85, v77, v85
	v_cvt_scalef32_pk_fp8_f32 v134, v66, v67, s36
	v_cvt_scalef32_pk_fp8_f32 v135, v70, v71, s36
	v_cvt_scalef32_pk_fp8_f32 v136, v74, v75, s36
	v_cvt_scalef32_pk_fp8_f32 v137, v78, v79, s36
	v_pk_add_f32 v[190:191], v[80:81], v[84:85]
	v_pk_add_f32 v[192:193], v[78:79], v[82:83]
	v_add_u32_e32 v106, s8, v218
	v_add_u32_e32 v107, s51, v183
	v_cvt_scalef32_pk_fp8_f32 v145, v148, v149, s36 op_sel:[0,0,0,1]
	v_cvt_scalef32_pk_fp8_f32 v134, v68, v69, s36 op_sel:[0,0,0,1]
	v_cvt_scalef32_pk_fp8_f32 v135, v72, v73, s36 op_sel:[0,0,0,1]
	v_cvt_scalef32_pk_fp8_f32 v136, v76, v77, s36 op_sel:[0,0,0,1]
	v_cvt_scalef32_pk_fp8_f32 v137, v80, v81, s36 op_sel:[0,0,0,1]
	s_waitcnt lgkmcnt(0)
	v_mfma_f32_32x32x64_f8f6f4 v[82:97], v[98:105], v[114:121], 0
	ds_read_b128 v[154:157], v234 offset:5120
	ds_read_b128 v[158:161], v234 offset:5136
	ds_read_b128 v[146:149], v234 offset:7680
	ds_read_b128 v[150:153], v234 offset:7696
	s_cmpk_gt_i32 s46, 0x1ff
	s_cbranch_scc1 .Lmy_rd1_ldum
	s_add_i32 s72, s61, -1
	s_cmp_lt_u32 s72, 12
	s_cbranch_scc0 .Lmy_rd1_noc
	s_waitcnt vmcnt(4)
	v_cvt_scalef32_pk_fp8_f32 v236, v236, v240, s62
	v_cvt_scalef32_pk_fp8_f32 v237, v237, v241, s62
	v_cvt_scalef32_pk_fp8_f32 v238, v238, v242, s62
	v_cvt_scalef32_pk_fp8_f32 v239, v239, v243, s62
	v_cvt_scalef32_pk_fp8_f32 v236, v244, v248, s62 op_sel:[0,0,0,1]
	v_cvt_scalef32_pk_fp8_f32 v237, v245, v249, s62 op_sel:[0,0,0,1]
	v_cvt_scalef32_pk_fp8_f32 v238, v246, v250, s62 op_sel:[0,0,0,1]
	v_cvt_scalef32_pk_fp8_f32 v239, v247, v251, s62 op_sel:[0,0,0,1]
	ds_write_b32 v252, v236
	ds_write_b32 v252, v237 offset:36
	ds_write_b32 v252, v238 offset:72
	ds_write_b32 v252, v239 offset:108

; DI void attn_unit_a8(unsigned char* lds, const AttnArgs& a) {
;     ...
;     auto w_decode = [&](int j, const float*& src, unsigned char*& dst, int& ld, int& n0, int& k0, bool& gu) __attribute__((always_inline)) {
;         const int g = (j >> 2) * 512 + a.wl, e = g / 96, rr = g - e * 96; KParamsPtr kp = kparams();
;         if (rr < 64) { src = kp->w_gu + ((size_t)a.wli * NE + e) * (1024 * 2048); dst = kp->ws + WS_WGU + (size_t)a.wli * SZ_WGU + (size_t)e * 2048 * 1024; ld = 2048; n0 = (rr & 7) * 256; k0 = ((rr >> 3) * 4 + (j & 3)) * 32; gu = true; }
;         else { const int q = rr - 64; src = kp->w_dn + ((size_t)a.wli * NE + e) * (1024 * 1024); dst = kp->ws + WS_WDN + (size_t)a.wli * SZ_WDN + (size_t)e * 1024 * 1024; ld = 1024; n0 = (q & 3) * 256; k0 = ((q >> 2) * 4 + (j & 3)) * 32; gu = false; } };
;     auto w_issue = [&](int j) __attribute__((always_inline)) { const float* src; unsigned char* dst; int ld, n0, k0; bool gu; w_decode(j, src, dst, ld, n0, k0, gu);
;         const float* p = src + (size_t)(k0 + 4 * wid) * ld + n0 + wn4;
;         wq[0] = __builtin_nontemporal_load((const f32x4*)p); wq[1] = __builtin_nontemporal_load((const f32x4*)(p + ld));
;         wq[2] = __builtin_nontemporal_load((const f32x4*)(p + (size_t)2 * ld)); wq[3] = __builtin_nontemporal_load((const f32x4*)(p + (size_t)3 * ld)); };
;     auto w_cvt = [&]() __attribute__((always_inline)) { unsigned char* t8 = lds + AT_WT + wn4 * WPITCH + 4 * wid;
; #pragma unroll
;         for (int j = 0; j < 4; ++j) *(unsigned*)(t8 + j * WPITCH) = pk4_fp8_mul64(wq[0][j], wq[1][j], wq[2][j], wq[3][j]); };
;     const int wcol = tid >> 1, whalf = tid & 1;
;     const unsigned wper_gu = (unsigned)((wcol >> 7) * 256 + (wcol & 96) + invperm32(wcol & 31)) * 1024u + 16u * whalf;
;     const unsigned wper_dn = (unsigned)fwd_lane16(wcol) * 1024u + 16u * whalf;
;     auto w_store = [&](int j) __attribute__((always_inline)) { const float* src; unsigned char* dst; int ld, n0, k0; bool gu; w_decode(j, src, dst, ld, n0, k0, gu);
;         const int nb = n0 >> 8; const unsigned uni = (unsigned)(gu ? (nb & 3) * 512 + (nb >> 2) * 128 : nb * 256) * 1024u + (unsigned)k0;
;         const unsigned off = (gu ? wper_gu : wper_dn) + uni;
;         const unsigned* t = (const unsigned*)(lds + AT_WT + wcol * WPITCH + 16 * whalf);
;         *(u32x4*)(dst + off) = (u32x4){t[0], t[1], t[2], t[3]}; };
.LBB0_1927:
	s_and_b32 s8, s19, 3
	s_add_i32 s8, s51, s8
	s_lshl_b32 s8, s8, 5
	s_add_i32 s8, s8, s20
	s_mul_hi_i32 s15, s12, s8
	s_mul_i32 s14, s12, s8
	s_lshl_b64 s[14:15], s[14:15], 2
	s_add_u32 s8, s10, s14
	s_addc_u32 s11, s11, s15
	s_lshl_b32 s10, s13, 2
	s_add_u32 s10, s8, s10
	s_addc_u32 s11, s11, 0
	s_cmp_lt_u32 s19, 12
	s_cbranch_scc1 .Lmy_a8l1
	s_load_dwordx2 s[10:11], s[0:1], 0xb0
	s_waitcnt lgkmcnt(0)
.Lmy_a8l1:
	s_lshl_b32 s8, s12, 2
	s_cmp_lt_u32 s19, 12
	s_cselect_b32 s8, s8, 0
	s_add_i32 s12, s18, 1
	s_cmp_lg_u32 s18, 2
	s_cselect_b32 s51, s12, 0
	s_mul_i32 s12, s51, 0x4680
	v_add_u32_e32 v176, s12, v169
	ds_read_b128 v[66:69], v176
	ds_read_b128 v[70:73], v176 offset:16
	v_lshl_add_u64 v[74:75], s[10:11], 0, v[106:107]
	v_lshl_add_u64 v[74:75], v[74:75], 0, s[8:9]
	v_lshl_add_u64 v[148:149], v[140:141], 0, v[132:133]
	global_load_dwordx4 v[116:119], v106, s[10:11] nt
	global_load_dwordx4 v[112:115], v[74:75], off nt
	v_lshl_add_u64 v[74:75], v[74:75], 0, s[8:9]
	s_waitcnt lgkmcnt(0)
	v_mfma_f32_32x32x64_f8f6f4 v[82:97], v[66:73], v[98:105], 0
	v_add_co_u32_e32 v66, vcc, s67, v148
	v_lshl_add_u64 v[76:77], v[74:75], 0, s[8:9]
	global_load_dwordx4 v[120:123], v[74:75], off nt
	global_load_dwordx4 v[124:127], v[76:77], off nt
	v_addc_co_u32_e32 v67, vcc, 0, v149, vcc
	v_lshl_add_u64 v[74:75], v[142:143], 0, v[132:133]
	v_add_co_u32_e32 v150, vcc, s68, v74
	s_mul_i32 s8, s18, 0x4680
	s_nop 0
	v_addc_co_u32_e32 v151, vcc, 0, v75, vcc
	v_add_u32_e32 v177, s8, v169
	global_load_dwordx2 v[144:145], v[66:67], off
	ds_read_b128 v[66:69], v176 offset:2560
	ds_read_b128 v[70:73], v176 offset:2576
	ds_read_b128 v[178:181], v177 offset:5120
	ds_read_b128 v[182:185], v177 offset:5136
	global_load_dwordx2 v[146:147], v[150:151], off offset:192
	v_exp_f32_e32 v164, v34
	v_exp_f32_e32 v165, v35
	v_exp_f32_e32 v154, v38
	v_exp_f32_e32 v155, v39
	v_exp_f32_e32 v162, v40
	v_exp_f32_e32 v163, v41
	v_exp_f32_e32 v158, v42
	v_exp_f32_e32 v159, v43
	v_exp_f32_e32 v46, v46
	v_exp_f32_e32 v47, v47
	v_exp_f32_e32 v50, v50
	v_exp_f32_e32 v51, v51
	v_exp_f32_e32 v40, v54
	v_exp_f32_e32 v41, v55
	v_exp_f32_e32 v42, v58
	v_exp_f32_e32 v43, v59
	v_exp_f32_e32 v34, v62
	v_exp_f32_e32 v35, v63
	v_exp_f32_e32 v160, v36
	v_exp_f32_e32 v161, v37
	v_exp_f32_e32 v152, v44
	v_exp_f32_e32 v153, v45
	v_exp_f32_e32 v156, v48
	v_exp_f32_e32 v157, v49
	v_exp_f32_e32 v44, v52
	v_exp_f32_e32 v45, v53
	v_exp_f32_e32 v48, v56
	v_exp_f32_e32 v49, v57
	v_exp_f32_e32 v36, v60
	v_exp_f32_e32 v37, v61
	v_exp_f32_e32 v38, v64
	v_exp_f32_e32 v39, v65
	s_nop 0
	s_nop 0
	s_nop 0
	s_nop 0
	s_nop 0
	s_nop 0
	s_nop 0
	s_nop 0
	v_cvt_scalef32_pk_fp8_f32 v52, v164, v165, s69
	v_cvt_scalef32_pk_fp8_f32 v56, v50, v51, s69
	v_cvt_scalef32_pk_fp8_f32 v53, v154, v155, s69
	v_cvt_scalef32_pk_fp8_f32 v57, v40, v41, s69
	v_cvt_scalef32_pk_fp8_f32 v54, v158, v159, s69
	v_cvt_scalef32_pk_fp8_f32 v58, v42, v43, s69
	v_cvt_scalef32_pk_fp8_f32 v55, v46, v47, s69
	v_cvt_scalef32_pk_fp8_f32 v59, v34, v35, s69
	v_cvt_scalef32_pk_fp8_f32 v52, v160, v161, s69 op_sel:[0,0,0,1]
	v_cvt_scalef32_pk_fp8_f32 v56, v44, v45, s69 op_sel:[0,0,0,1]
	v_cvt_scalef32_pk_fp8_f32 v53, v162, v163, s69 op_sel:[0,0,0,1]
	v_cvt_scalef32_pk_fp8_f32 v57, v48, v49, s69 op_sel:[0,0,0,1]
	v_cvt_scalef32_pk_fp8_f32 v54, v152, v153, s69 op_sel:[0,0,0,1]
	v_cvt_scalef32_pk_fp8_f32 v58, v36, v37, s69 op_sel:[0,0,0,1]
	v_cvt_scalef32_pk_fp8_f32 v55, v156, v157, s69 op_sel:[0,0,0,1]
	v_cvt_scalef32_pk_fp8_f32 v59, v38, v39, s69 op_sel:[0,0,0,1]
	s_add_i32 s8, s12, 0x4680
	s_cmp_eq_u32 s51, 2
	s_waitcnt lgkmcnt(0)
	v_mfma_f32_32x32x64_f8f6f4 v[18:33], v[178:185], v[52:59], v[18:33]
	ds_read_b128 v[178:181], v177 offset:7680
	ds_read_b128 v[182:185], v177 offset:7696
	s_cselect_b64 s[12:13], -1, 0
	s_and_b64 s[10:11], s[12:13], exec
	s_cselect_b32 s8, 0, s8
	s_add_i32 s8, s8, 0
	s_mov_b64 s[18:19], -1
	v_mfma_f32_32x32x64_f8f6f4 v[66:81], v[66:73], v[98:105], 0
	s_waitcnt lgkmcnt(0)
	v_mfma_f32_32x32x64_f8f6f4 v[2:17], v[178:185], v[52:59], v[2:17]
	v_add_u32_e32 v52, s8, v131
	s_waitcnt vmcnt(7)
	ds_write_b64 v52, v[136:137]
	v_add_u32_e32 v52, s8, v168
	s_and_b32 s8, s23, 0xe00
	s_add_i32 s10, s8, s76
	s_mul_hi_u32 s8, s10, 0xaaaaaaab
	s_lshr_b32 s8, s8, 6
	s_mul_i32 s53, s8, 0xffffffa0
	v_add_u32_e32 v52, 0x1400, v52
	s_add_i32 s53, s53, s10
	s_mov_b64 s[10:11], s[0:1]
	s_waitcnt vmcnt(6)
	ds_write2_b32 v52, v138, v139 offset1:8
	s_waitcnt lgkmcnt(0)
	s_barrier
	s_load_dwordx2 s[16:17], s[10:11], 0xd8
	s_cmp_lt_i32 s53, 64
	s_cselect_b64 s[14:15], -1, 0
	s_cmp_gt_i32 s53, 63
	s_cbranch_scc0 .LBB0_1929
	s_lshl_b64 s[10:11], s[8:9], 20
	s_waitcnt lgkmcnt(0)
	s_add_u32 s10, s16, s10
	s_addc_u32 s11, s17, s11
	s_add_u32 s10, s10, 0x15094000
	s_addc_u32 s11, s11, 0
	s_cmp_lt_u32 s50, 12
	s_cbranch_scc1 .Lmy_a8s1d
	s_add_u32 s10, s16, 0x1c094000
	s_addc_u32 s11, s17, 0
.Lmy_a8s1d:
	s_and_b32 s18, s53, 0x7ffffffc
	s_sub_i32 s52, s18, 64
	s_mov_b64 s[18:19], 0
.LBB0_1929:
	s_andn2_b64 vcc, exec, s[18:19]
	v_mov_b32_e32 v52, v173
	s_mov_b32 s18, s21
	s_cbranch_vccnz .LBB0_1922
	s_lshl_b64 s[10:11], s[8:9], 21
	s_waitcnt lgkmcnt(0)
	s_add_u32 s8, s16, s10
	s_addc_u32 s11, s17, s11
	s_add_u32 s10, s8, 0x9094000
	s_addc_u32 s11, s11, 0
	s_cmp_lt_u32 s50, 12
	s_cbranch_scc1 .Lmy_a8s1g
	s_add_u32 s10, s16, 0x1c094000
	s_addc_u32 s11, s17, 0
.Lmy_a8s1g:
	s_ashr_i32 s8, s53, 1
	s_and_b32 s52, s8, -4
	v_mov_b32_e32 v52, v171
	s_mov_b32 s18, s22
	s_branch .LBB0_1922
